# stack: queue-index lookahead + mLSTM-out early gate loads + coalesced qk-norm units + router weight tile copy with 12 loads in flight
# baseline (speedup 1.0000x reference)
; #define LAS __attribute__((address_space(3)))
; DI void tile_g2l(LAS bf16* dst, int lp, const bf16* src, size_t gp, int rows, int cols, int tid) {
;     const int cpr = cols >> 3, n = rows * cpr;
;     if (n % (4 * NWAVES * 64) == 0) {
;         for (int i0 = tid; i0 < n; i0 += 4 * NWAVES * 64) { v4u t[4];
; #pragma unroll
;             for (int j = 0; j < 4; ++j) { const int i = i0 + j * NWAVES * 64, r = i / cpr, c = (i % cpr) * 8; t[j] = *(const v4u*)(src + (size_t)r * gp + c); }
; #pragma unroll
;             for (int j = 0; j < 4; ++j) { const int i = i0 + j * NWAVES * 64, r = i / cpr, c = (i % cpr) * 8; *(LAS v4u*)(dst + r * lp + c) = t[j]; } }
;         return; }
; DI void p_router(Frame& F, int l) {
;     ...
;     LAS bf16* WRL = (LAS bf16*)F.lds;
;     LAS float* LG = (LAS float*)(F.lds + 48 * WRP * 2);
;     LAS int* CNT = (LAS int*)(F.lds + 48 * WRP * 2 + 8 * 16 * 48 * 4);
;     const bf16* H = (const bf16*)(F.ws + WS_H); const bf16* WR = (const bf16*)(F.ws + WS_WR);
;     int* tok_e = (int*)(F.ws + WS_TOK); int* tok_lp = (int*)(F.ws + WS_TOK + 256 * 1024); float* tok_w = (float*)(F.ws + WS_TOK + 512 * 1024);
;     int* hist = (int*)(F.ws + WS_SMALL + 192 * 1024);
;     const int r = F.lane & 15, q = F.lane >> 4;
;     tile_g2l(WRL, WRP, WR, 1024, 48, 1024, F.tid);
;     __syncthreads();
.LBB0_3291:
	v_readlane_b32 s2, v255, 10
	s_cmp_le_i32 s2, s50
	s_cselect_b64 s[12:13], -1, 0
	s_and_b64 s[0:1], s[12:13], s[0:1]
	s_andn2_b64 vcc, exec, s[0:1]
	v_readlane_b32 s3, v255, 11
	s_cbranch_vccnz .LBB0_3378
	v_mov_b32_e32 v1, v228
	s_mov_b64 s[0:1], 0
	s_mov_b32 s2, s53
	v_readlane_b32 s52, v255, 2
	s_and_b32 s42, s57, 7
	s_lshl_b32 s42, s42, 5
	s_lshr_b32 s43, s57, 3
	s_add_i32 s42, s42, s43
	v_readlane_b32 s4, v255, 3
	s_add_i32 s94, s2, 0
	v_readlane_b32 s6, v255, 5
	v_readlane_b32 s7, v255, 6
	s_add_u32 s0, s6, s0
	s_movk_i32 s2, 0x1800
	v_readfirstlane_b32 s9, v1
	s_addc_u32 s1, s7, s1
	v_readlane_b32 s8, v255, 19
	v_cmp_gt_i32_e32 vcc, s2, v1
	v_readlane_b32 s5, v255, 4
	s_and_saveexec_b64 s[2:3], vcc
	s_movk_i32 s11, 0x810
	s_cbranch_execz .LBB0_3295
	s_add_u32 s4, s0, 0x700000
	s_addc_u32 s5, s1, 0
	s_movk_i32 s10, 0xfff
	s_waitcnt lgkmcnt(0)
	v_lshlrev_b32_e32 v2, 4, v1
	v_lshrrev_b32_e32 v4, 7, v1
	v_mul_u32_u24_e32 v4, 0x810, v4
	v_and_b32_e32 v5, 0x7f, v1
	v_lshl_add_u32 v4, v5, 4, v4
	v_add_u32_e32 v4, s94, v4
	v_add_u32_e32 v5, 0x10200, v4
	s_waitcnt vmcnt(0)
	global_load_dwordx4 v[152:155], v2, s[4:5]
	v_add_u32_e32 v2, 0x2000, v2
	global_load_dwordx4 v[156:159], v2, s[4:5]
	v_add_u32_e32 v2, 0x2000, v2
	global_load_dwordx4 v[160:163], v2, s[4:5]
	v_add_u32_e32 v2, 0x2000, v2
	global_load_dwordx4 v[164:167], v2, s[4:5]
	v_add_u32_e32 v2, 0x2000, v2
	global_load_dwordx4 v[168:171], v2, s[4:5]
	v_add_u32_e32 v2, 0x2000, v2
	global_load_dwordx4 v[172:175], v2, s[4:5]
	v_add_u32_e32 v2, 0x2000, v2
	global_load_dwordx4 v[176:179], v2, s[4:5]
	v_add_u32_e32 v2, 0x2000, v2
	global_load_dwordx4 v[180:183], v2, s[4:5]
	v_add_u32_e32 v2, 0x2000, v2
	global_load_dwordx4 v[184:187], v2, s[4:5]
	v_add_u32_e32 v2, 0x2000, v2
	global_load_dwordx4 v[188:191], v2, s[4:5]
	v_add_u32_e32 v2, 0x2000, v2
	global_load_dwordx4 v[192:195], v2, s[4:5]
	v_add_u32_e32 v2, 0x2000, v2
	global_load_dwordx4 v[196:199], v2, s[4:5]
	s_waitcnt vmcnt(11)
	ds_write_b128 v4, v[152:155]
	s_waitcnt vmcnt(10)
	ds_write_b128 v4, v[156:159] offset:8256
	s_waitcnt vmcnt(9)
	ds_write_b128 v4, v[160:163] offset:16512
	s_waitcnt vmcnt(8)
	ds_write_b128 v4, v[164:167] offset:24768
	s_waitcnt vmcnt(7)
	ds_write_b128 v4, v[168:171] offset:33024
	s_waitcnt vmcnt(6)
	ds_write_b128 v4, v[172:175] offset:41280
	s_waitcnt vmcnt(5)
	ds_write_b128 v4, v[176:179] offset:49536
	s_waitcnt vmcnt(4)
	ds_write_b128 v4, v[180:183] offset:57792
	s_waitcnt vmcnt(3)
	ds_write_b128 v5, v[184:187]
	s_waitcnt vmcnt(2)
	ds_write_b128 v5, v[188:191] offset:8256
	s_waitcnt vmcnt(1)
	ds_write_b128 v5, v[192:195] offset:16512
	s_waitcnt vmcnt(0)
	ds_write_b128 v5, v[196:199] offset:24768
